# exp2: per-unit (weight,dst) rows prefetched by one early load per thread into an LDS table; epilogue reads them with ds_read_b64 instead of 8 global loads + vmcnt(0)
# speedup vs baseline: 1.0086x; 1.0069x over previous
.LBB0_3603:
	v_readlane_b32 s0, v255, 0
	v_readlane_b32 s1, v255, 1
	s_andn2_b64 vcc, exec, s[0:1]
	s_cbranch_vccnz .LBB0_3649
	s_mov_b32 s3, s40
	s_lshl_b64 s[0:1], s[2:3], 2
	v_readlane_b32 s2, v254, 58
	v_readlane_b32 s3, v254, 59
	s_add_u32 s33, s2, s0
	s_mov_b32 s43, s40
	s_addc_u32 s36, s3, s1
	s_lshl_b64 s[0:1], s[42:43], 3
	v_readlane_b32 s2, v255, 4
	v_readlane_b32 s3, v255, 5
	s_add_u32 s0, s2, s0
	s_addc_u32 s1, s3, s1
	s_lshl_b32 s4, s81, 3
	s_cmp_lt_i32 s92, s4
	s_cselect_b64 s[2:3], -1, 0
	v_writelane_b32 v254, s2, 42
	s_nop 1
	v_writelane_b32 v254, s3, 43
	s_mov_b32 s2, 0
	v_readlane_b32 s3, v254, 40
	s_cmp_lt_i32 s3, s81
	s_cselect_b64 s[8:9], -1, 0
	v_writelane_b32 v254, s8, 44
	s_nop 1
	v_writelane_b32 v254, s9, 45
	v_mbcnt_lo_u32_b32 v242, -1, 0
	v_mbcnt_hi_u32_b32 v242, -1, v242
	s_and_b32 s8, s92, 7
	s_lshl_b32 s8, s8, 2
	s_bfe_u32 s9, s92, 0x20003
	s_add_i32 s8, s8, s9
	v_lshl_add_u32 v242, v242, 5, s8
	v_lshlrev_b32_e32 v242, 2, v242
	s_mov_b32 s8, s33
	s_mov_b32 s9, s36
	s_nop 0
	global_load_dword v242, v242, s[8:9]
	s_waitcnt vmcnt(0)
	v_and_b32_e32 v249, 0xff, v0
	v_lshlrev_b32_e32 v248, 3, v249
	v_add_u32_e32 v248, 0x20000, v248
	s_nop 0
	s_nop 0
	s_branch .LBB0_3607

.LBB0_3625:
	s_ashr_i32 s23, s22, 31
	s_lshl_b64 s[26:27], s[22:23], 17
	s_add_u32 s34, s66, s26
	s_addc_u32 s35, s67, s27
	s_and_b64 s[26:27], s[16:17], exec
	s_cselect_b32 s29, s35, s19
	s_cselect_b32 s28, s34, s18
	s_lshl_b32 s26, s60, 8
	s_ashr_i32 s25, s24, 31
	s_ashr_i32 s27, s26, 31
	s_lshl_b64 s[30:31], s[24:25], 20
	s_lshl_b64 s[26:27], s[26:27], 9
	s_add_u32 s13, s39, s30
	s_addc_u32 s23, s80, s31
	s_add_u32 s30, s13, s26
	s_addc_u32 s31, s23, s27
	s_and_b64 s[26:27], s[16:17], exec
	s_cselect_b32 s27, s31, s21
	s_cselect_b32 s26, s30, s20
	s_add_i32 s23, 0, 0x10000
	v_add_u32_e32 v142, s23, v215
	ds_read_b128 v[6:9], v142
	ds_read_b128 v[10:13], v142 offset:1024
	s_waitcnt vmcnt(0)
	ds_read_b128 v[164:167], v142 offset:2048
	ds_read_b128 v[168:171], v142 offset:3072
	s_mov_b64 vcc, -1
	v_lshl_add_u64 v[130:131], s[18:19], 0, v[154:155]
	s_add_i32 s61, s15, 0xc000
	v_lshl_add_u64 v[2:3], v[130:131], 0, s[44:45]
	s_mov_b32 m0, s61
	v_lshl_add_u64 v[132:133], s[18:19], 0, v[156:157]
	s_add_i32 s13, s15, 0xe000
	ds_read_b128 v[14:17], v217
	ds_read_b128 v[18:21], v217 offset:1024
	ds_read_b128 v[22:25], v217 offset:2048
	ds_read_b128 v[26:29], v217 offset:3072
	ds_read_b128 v[30:33], v217 offset:4096
	ds_read_b128 v[34:37], v217 offset:5120
	ds_read_b128 v[38:41], v217 offset:6144
	ds_read_b128 v[42:45], v217 offset:7168
	global_load_lds_dwordx4 v[2:3], off
	v_lshl_add_u64 v[2:3], v[132:133], 0, s[44:45]
	s_mov_b32 m0, s13
	s_nop 0
	global_load_lds_dwordx4 v[2:3], off
	v_lshl_add_u32 v246, s14, 8, v249
	v_ashrrev_i32_e32 v247, 31, v246
	v_lshl_add_u64 v[246:247], v[246:247], 3, s[0:1]
	global_load_dwordx2 v[244:245], v[246:247], off
	s_waitcnt lgkmcnt(8)
	s_barrier
	s_waitcnt lgkmcnt(0)
	s_setprio 1
	s_mov_b32 s41, s40
	s_mov_b32 s42, s40
	s_mov_b32 s43, s40
	v_mov_b64_e32 v[2:3], s[40:41]
	v_mov_b64_e32 v[120:121], s[42:43]
	v_mov_b64_e32 v[116:117], s[42:43]
	v_mov_b64_e32 v[104:105], s[42:43]
	v_mov_b64_e32 v[100:101], s[42:43]
	v_mov_b64_e32 v[88:89], s[42:43]
	v_mov_b64_e32 v[84:85], s[42:43]
	v_mov_b64_e32 v[60:61], s[42:43]
	v_mov_b64_e32 v[52:53], s[42:43]
	v_mov_b64_e32 v[4:5], s[42:43]
	v_mov_b64_e32 v[118:119], s[40:41]
	v_mov_b64_e32 v[114:115], s[40:41]
	v_mov_b64_e32 v[102:103], s[40:41]
	v_mov_b64_e32 v[98:99], s[40:41]
	v_mov_b64_e32 v[86:87], s[40:41]
	v_mov_b64_e32 v[82:83], s[40:41]
	v_mov_b64_e32 v[58:59], s[40:41]
	v_mov_b64_e32 v[50:51], s[40:41]
	s_waitcnt lgkmcnt(0)
	v_mfma_scale_f32_16x16x128_f8f6f4 v[118:121], v[6:13], v[14:21], v[118:121], v210, v210 op_sel_hi:[0,0,0]
	v_mfma_scale_f32_16x16x128_f8f6f4 v[114:117], v[164:171], v[14:21], v[114:117], v210, v210 op_sel_hi:[0,0,0]
	v_mfma_scale_f32_16x16x128_f8f6f4 v[102:105], v[6:13], v[22:29], v[102:105], v210, v210 op_sel_hi:[0,0,0]
	v_mfma_scale_f32_16x16x128_f8f6f4 v[98:101], v[164:171], v[22:29], v[98:101], v210, v210 op_sel_hi:[0,0,0]
	v_mfma_scale_f32_16x16x128_f8f6f4 v[86:89], v[6:13], v[30:37], v[86:89], v210, v210 op_sel_hi:[0,0,0]
	v_mfma_scale_f32_16x16x128_f8f6f4 v[82:85], v[164:171], v[30:37], v[82:85], v210, v210 op_sel_hi:[0,0,0]
	v_mfma_scale_f32_16x16x128_f8f6f4 v[58:61], v[6:13], v[38:45], v[58:61], v210, v210 op_sel_hi:[0,0,0]
	v_mfma_scale_f32_16x16x128_f8f6f4 v[50:53], v[164:171], v[38:45], v[50:53], v210, v210 op_sel_hi:[0,0,0]
	s_setprio 0
	s_barrier
	s_add_i32 s25, 0, 0x14000
	v_lshl_add_u64 v[134:135], s[20:21], 0, v[146:147]
	s_add_i32 s41, s23, s87
	v_add_u32_e32 v143, s25, v215
	v_lshl_add_u64 v[46:47], v[134:135], 0, s[84:85]
	s_mov_b32 m0, s41
	v_lshl_add_u64 v[136:137], s[20:21], 0, v[148:149]
	s_add_i32 s23, s41, 0x2000
	ds_read_b128 v[172:175], v143
	ds_read_b128 v[176:179], v143 offset:1024
	ds_read_b128 v[180:183], v143 offset:2048
	ds_read_b128 v[184:187], v143 offset:3072
	global_load_lds_dwordx4 v[46:47], off
	v_lshl_add_u64 v[46:47], v[136:137], 0, s[84:85]
	s_mov_b32 m0, s23
	s_nop 0
	global_load_lds_dwordx4 v[46:47], off
	s_barrier
	s_waitcnt lgkmcnt(0)
	s_setprio 1
	v_mov_b64_e32 v[128:129], v[4:5]
	v_mov_b64_e32 v[124:125], v[4:5]
	v_mov_b64_e32 v[112:113], v[4:5]
	v_mov_b64_e32 v[108:109], v[4:5]
	v_mov_b64_e32 v[96:97], v[4:5]
	v_mov_b64_e32 v[92:93], v[4:5]
	v_mov_b64_e32 v[80:81], v[4:5]
	v_mov_b64_e32 v[76:77], v[4:5]
	v_mov_b64_e32 v[126:127], v[2:3]
	v_mov_b64_e32 v[122:123], v[2:3]
	v_mov_b64_e32 v[110:111], v[2:3]
	v_mov_b64_e32 v[106:107], v[2:3]
	v_mov_b64_e32 v[94:95], v[2:3]
	v_mov_b64_e32 v[90:91], v[2:3]
	v_mov_b64_e32 v[78:79], v[2:3]
	v_mov_b64_e32 v[74:75], v[2:3]
	s_waitcnt lgkmcnt(0)
	v_mfma_scale_f32_16x16x128_f8f6f4 v[126:129], v[172:179], v[14:21], v[126:129], v210, v210 op_sel_hi:[0,0,0]
	v_mfma_scale_f32_16x16x128_f8f6f4 v[122:125], v[180:187], v[14:21], v[122:125], v210, v210 op_sel_hi:[0,0,0]
	v_mfma_scale_f32_16x16x128_f8f6f4 v[110:113], v[172:179], v[22:29], v[110:113], v210, v210 op_sel_hi:[0,0,0]
	v_mfma_scale_f32_16x16x128_f8f6f4 v[106:109], v[180:187], v[22:29], v[106:109], v210, v210 op_sel_hi:[0,0,0]
	v_mfma_scale_f32_16x16x128_f8f6f4 v[94:97], v[172:179], v[30:37], v[94:97], v210, v210 op_sel_hi:[0,0,0]
	v_mfma_scale_f32_16x16x128_f8f6f4 v[90:93], v[180:187], v[30:37], v[90:93], v210, v210 op_sel_hi:[0,0,0]
	v_mfma_scale_f32_16x16x128_f8f6f4 v[78:81], v[172:179], v[38:45], v[78:81], v210, v210 op_sel_hi:[0,0,0]
	v_mfma_scale_f32_16x16x128_f8f6f4 v[74:77], v[180:187], v[38:45], v[74:77], v210, v210 op_sel_hi:[0,0,0]
	s_setprio 0
	v_lshl_add_u64 v[138:139], s[18:19], 0, v[150:151]
	s_mov_b32 m0, s15
	v_lshl_add_u64 v[14:15], v[138:139], 0, s[84:85]
	v_lshl_add_u64 v[140:141], s[18:19], 0, v[152:153]
	s_barrier
	ds_read_b128 v[188:191], v217 offset:16384
	ds_read_b128 v[192:195], v217 offset:17408
	ds_read_b128 v[196:199], v217 offset:18432
	ds_read_b128 v[200:203], v217 offset:19456
	ds_read_b128 v[218:221], v217 offset:20480
	ds_read_b128 v[222:225], v217 offset:21504
	ds_read_b128 v[226:229], v217 offset:22528
	ds_read_b128 v[230:233], v217 offset:23552
	global_load_lds_dwordx4 v[14:15], off
	v_lshl_add_u64 v[14:15], v[140:141], 0, s[84:85]
	s_mov_b32 m0, s8
	s_nop 0
	global_load_lds_dwordx4 v[14:15], off
	s_barrier
	s_waitcnt lgkmcnt(0)
	s_setprio 1
	v_mov_b64_e32 v[72:73], v[4:5]
	v_mov_b64_e32 v[64:65], v[4:5]
	v_mov_b64_e32 v[48:49], v[4:5]
	v_mov_b64_e32 v[40:41], v[4:5]
	v_mov_b64_e32 v[32:33], v[4:5]
	v_mov_b64_e32 v[24:25], v[4:5]
	v_mov_b64_e32 v[16:17], v[4:5]
	v_mov_b64_e32 v[70:71], v[2:3]
	v_mov_b64_e32 v[62:63], v[2:3]
	v_mov_b64_e32 v[46:47], v[2:3]
	v_mov_b64_e32 v[38:39], v[2:3]
	v_mov_b64_e32 v[30:31], v[2:3]
	v_mov_b64_e32 v[22:23], v[2:3]
	v_mov_b64_e32 v[14:15], v[2:3]
	s_waitcnt lgkmcnt(0)
	v_mfma_scale_f32_16x16x128_f8f6f4 v[70:73], v[6:13], v[188:195], v[70:73], v210, v210 op_sel_hi:[0,0,0]
	v_mfma_scale_f32_16x16x128_f8f6f4 v[62:65], v[164:171], v[188:195], v[62:65], v210, v210 op_sel_hi:[0,0,0]
	v_mfma_scale_f32_16x16x128_f8f6f4 v[46:49], v[6:13], v[196:203], v[46:49], v210, v210 op_sel_hi:[0,0,0]
	v_mfma_scale_f32_16x16x128_f8f6f4 v[38:41], v[164:171], v[196:203], v[38:41], v210, v210 op_sel_hi:[0,0,0]
	v_mfma_scale_f32_16x16x128_f8f6f4 v[30:33], v[6:13], v[218:225], v[30:33], v210, v210 op_sel_hi:[0,0,0]
	v_mfma_scale_f32_16x16x128_f8f6f4 v[22:25], v[164:171], v[218:225], v[22:25], v210, v210 op_sel_hi:[0,0,0]
	v_mfma_scale_f32_16x16x128_f8f6f4 v[14:17], v[6:13], v[226:233], v[14:17], v210, v210 op_sel_hi:[0,0,0]
	v_mov_b64_e32 v[8:9], v[4:5]
	v_mov_b64_e32 v[6:7], v[2:3]
	v_mfma_scale_f32_16x16x128_f8f6f4 v[6:9], v[164:171], v[226:233], v[6:9], v210, v210 op_sel_hi:[0,0,0]
	s_setprio 0
	s_barrier
	s_add_u32 s42, s20, 0x10100
	s_addc_u32 s43, s21, 0
	s_add_i32 s19, s25, s87
	v_lshl_add_u64 v[10:11], s[42:43], 0, v[146:147]
	s_mov_b32 m0, s19
	s_add_i32 s18, s19, 0x2000
	global_load_lds_dwordx4 v[10:11], off
	v_lshl_add_u64 v[10:11], s[42:43], 0, v[148:149]
	s_mov_b32 m0, s18
	s_nop 0
	global_load_lds_dwordx4 v[10:11], off
	s_waitcnt vmcnt(6)
	ds_write_b64 v248, v[244:245]
	s_barrier
	s_setprio 1
	v_mov_b64_e32 v[68:69], v[4:5]
	v_mov_b64_e32 v[56:57], v[4:5]
	v_mov_b64_e32 v[44:45], v[4:5]
	v_mov_b64_e32 v[36:37], v[4:5]
	v_mov_b64_e32 v[28:29], v[4:5]
	v_mov_b64_e32 v[20:21], v[4:5]
	v_mov_b64_e32 v[12:13], v[4:5]
	v_mov_b64_e32 v[66:67], v[2:3]
	v_mov_b64_e32 v[54:55], v[2:3]
	v_mov_b64_e32 v[42:43], v[2:3]
	v_mov_b64_e32 v[34:35], v[2:3]
	v_mov_b64_e32 v[26:27], v[2:3]
	v_mov_b64_e32 v[18:19], v[2:3]
	v_mov_b64_e32 v[10:11], v[2:3]
	v_mfma_scale_f32_16x16x128_f8f6f4 v[66:69], v[172:179], v[188:195], v[66:69], v210, v210 op_sel_hi:[0,0,0]
	v_mfma_scale_f32_16x16x128_f8f6f4 v[54:57], v[180:187], v[188:195], v[54:57], v210, v210 op_sel_hi:[0,0,0]
	v_mfma_scale_f32_16x16x128_f8f6f4 v[42:45], v[172:179], v[196:203], v[42:45], v210, v210 op_sel_hi:[0,0,0]
	v_mfma_scale_f32_16x16x128_f8f6f4 v[34:37], v[180:187], v[196:203], v[34:37], v210, v210 op_sel_hi:[0,0,0]
	v_mfma_scale_f32_16x16x128_f8f6f4 v[26:29], v[172:179], v[218:225], v[26:29], v210, v210 op_sel_hi:[0,0,0]
	v_mfma_scale_f32_16x16x128_f8f6f4 v[18:21], v[180:187], v[218:225], v[18:21], v210, v210 op_sel_hi:[0,0,0]
	v_mfma_scale_f32_16x16x128_f8f6f4 v[10:13], v[172:179], v[226:233], v[10:13], v210, v210 op_sel_hi:[0,0,0]
	v_mfma_scale_f32_16x16x128_f8f6f4 v[2:5], v[180:187], v[226:233], v[2:5], v210, v210 op_sel_hi:[0,0,0]
	s_setprio 0
	s_add_i32 s42, 0, 0x18000
	v_add_u32_e32 v144, s42, v215
	s_barrier
	ds_read_b128 v[164:167], v144
	ds_read_b128 v[168:171], v144 offset:1024
	ds_read_b128 v[172:175], v144 offset:2048
	ds_read_b128 v[176:179], v144 offset:3072
	s_mov_b32 m0, s9
	v_lshl_add_u64 v[160:161], v[130:131], 0, s[84:85]
	ds_read_b128 v[180:183], v217 offset:32768
	ds_read_b128 v[184:187], v217 offset:33792
	ds_read_b128 v[188:191], v217 offset:34816
	ds_read_b128 v[192:195], v217 offset:35840
	ds_read_b128 v[196:199], v217 offset:36864
	ds_read_b128 v[200:203], v217 offset:37888
	ds_read_b128 v[218:221], v217 offset:38912
	ds_read_b128 v[222:225], v217 offset:39936
	global_load_lds_dwordx4 v[160:161], off
	v_lshl_add_u64 v[160:161], v[132:133], 0, s[84:85]
	s_mov_b32 m0, s82
	s_nop 0
	global_load_lds_dwordx4 v[160:161], off
	s_waitcnt lgkmcnt(8)
	s_barrier
	s_waitcnt lgkmcnt(0)
	s_setprio 1
	s_waitcnt lgkmcnt(0)
	v_mfma_scale_f32_16x16x128_f8f6f4 v[118:121], v[164:171], v[180:187], v[118:121], v210, v210 op_sel_hi:[0,0,0]
	v_mfma_scale_f32_16x16x128_f8f6f4 v[114:117], v[172:179], v[180:187], v[114:117], v210, v210 op_sel_hi:[0,0,0]
	v_mfma_scale_f32_16x16x128_f8f6f4 v[102:105], v[164:171], v[188:195], v[102:105], v210, v210 op_sel_hi:[0,0,0]
	v_mfma_scale_f32_16x16x128_f8f6f4 v[98:101], v[172:179], v[188:195], v[98:101], v210, v210 op_sel_hi:[0,0,0]
	v_mfma_scale_f32_16x16x128_f8f6f4 v[86:89], v[164:171], v[196:203], v[86:89], v210, v210 op_sel_hi:[0,0,0]
	v_mfma_scale_f32_16x16x128_f8f6f4 v[82:85], v[172:179], v[196:203], v[82:85], v210, v210 op_sel_hi:[0,0,0]
	v_mfma_scale_f32_16x16x128_f8f6f4 v[58:61], v[164:171], v[218:225], v[58:61], v210, v210 op_sel_hi:[0,0,0]
	v_mfma_scale_f32_16x16x128_f8f6f4 v[50:53], v[172:179], v[218:225], v[50:53], v210, v210 op_sel_hi:[0,0,0]
	s_setprio 0
	s_barrier
	s_add_i32 s43, 0, 0x1c000
	s_add_i32 s42, s42, s87
	v_add_u32_e32 v145, s43, v215
	v_lshl_add_u64 v[134:135], v[134:135], 0, s[58:59]
	s_mov_b32 m0, s42
	s_add_i32 s25, s42, 0x2000
	ds_read_b128 v[226:229], v145
	ds_read_b128 v[230:233], v145 offset:1024
	ds_read_b128 v[234:237], v145 offset:2048
	ds_read_b128 v[238:241], v145 offset:3072
	global_load_lds_dwordx4 v[134:135], off
	v_lshl_add_u64 v[134:135], v[136:137], 0, s[58:59]
	s_mov_b32 m0, s25
	s_nop 0
	global_load_lds_dwordx4 v[134:135], off
	s_barrier
	s_waitcnt lgkmcnt(0)
	s_setprio 1
	s_waitcnt lgkmcnt(0)
	v_mfma_scale_f32_16x16x128_f8f6f4 v[126:129], v[226:233], v[180:187], v[126:129], v210, v210 op_sel_hi:[0,0,0]
	v_mfma_scale_f32_16x16x128_f8f6f4 v[122:125], v[234:241], v[180:187], v[122:125], v210, v210 op_sel_hi:[0,0,0]
	v_mfma_scale_f32_16x16x128_f8f6f4 v[110:113], v[226:233], v[188:195], v[110:113], v210, v210 op_sel_hi:[0,0,0]
	v_mfma_scale_f32_16x16x128_f8f6f4 v[106:109], v[234:241], v[188:195], v[106:109], v210, v210 op_sel_hi:[0,0,0]
	v_mfma_scale_f32_16x16x128_f8f6f4 v[94:97], v[226:233], v[196:203], v[94:97], v210, v210 op_sel_hi:[0,0,0]
	v_mfma_scale_f32_16x16x128_f8f6f4 v[90:93], v[234:241], v[196:203], v[90:93], v210, v210 op_sel_hi:[0,0,0]
	v_mfma_scale_f32_16x16x128_f8f6f4 v[78:81], v[226:233], v[218:225], v[78:81], v210, v210 op_sel_hi:[0,0,0]
	v_mfma_scale_f32_16x16x128_f8f6f4 v[74:77], v[234:241], v[218:225], v[74:77], v210, v210 op_sel_hi:[0,0,0]
	s_setprio 0
	s_mov_b32 m0, s83
	v_lshl_add_u64 v[134:135], v[138:139], 0, s[58:59]
	s_barrier
	ds_read_b128 v[180:183], v217 offset:49152
	ds_read_b128 v[184:187], v217 offset:50176
	ds_read_b128 v[188:191], v217 offset:51200
	ds_read_b128 v[192:195], v217 offset:52224
	ds_read_b128 v[196:199], v217 offset:53248
	ds_read_b128 v[200:203], v217 offset:54272
	ds_read_b128 v[218:221], v217 offset:55296
	ds_read_b128 v[222:225], v217 offset:56320
	global_load_lds_dwordx4 v[134:135], off
	v_lshl_add_u64 v[134:135], v[140:141], 0, s[58:59]
	s_mov_b32 m0, s5
	s_nop 0
	global_load_lds_dwordx4 v[134:135], off
	s_barrier
	s_waitcnt lgkmcnt(0)
	s_setprio 1
	s_waitcnt lgkmcnt(0)
	v_mfma_scale_f32_16x16x128_f8f6f4 v[70:73], v[164:171], v[180:187], v[70:73], v210, v210 op_sel_hi:[0,0,0]
	v_mfma_scale_f32_16x16x128_f8f6f4 v[62:65], v[172:179], v[180:187], v[62:65], v210, v210 op_sel_hi:[0,0,0]
	v_mfma_scale_f32_16x16x128_f8f6f4 v[46:49], v[164:171], v[188:195], v[46:49], v210, v210 op_sel_hi:[0,0,0]
	v_mfma_scale_f32_16x16x128_f8f6f4 v[38:41], v[172:179], v[188:195], v[38:41], v210, v210 op_sel_hi:[0,0,0]
	v_mfma_scale_f32_16x16x128_f8f6f4 v[30:33], v[164:171], v[196:203], v[30:33], v210, v210 op_sel_hi:[0,0,0]
	v_mfma_scale_f32_16x16x128_f8f6f4 v[22:25], v[172:179], v[196:203], v[22:25], v210, v210 op_sel_hi:[0,0,0]
	v_mfma_scale_f32_16x16x128_f8f6f4 v[14:17], v[164:171], v[218:225], v[14:17], v210, v210 op_sel_hi:[0,0,0]
	v_mfma_scale_f32_16x16x128_f8f6f4 v[6:9], v[172:179], v[218:225], v[6:9], v210, v210 op_sel_hi:[0,0,0]
	s_setprio 0
	s_barrier
	s_add_u32 s90, s20, 0x10180
	s_addc_u32 s91, s21, 0
	s_add_i32 s21, s43, s87
	v_lshl_add_u64 v[134:135], s[90:91], 0, v[146:147]
	s_mov_b32 m0, s21
	s_add_i32 s20, s21, 0x2000
	global_load_lds_dwordx4 v[134:135], off
	v_lshl_add_u64 v[134:135], s[90:91], 0, v[148:149]
	s_mov_b32 m0, s20
	s_nop 0
	global_load_lds_dwordx4 v[134:135], off
	s_waitcnt vmcnt(6)
	s_barrier
	s_setprio 1
	v_mfma_scale_f32_16x16x128_f8f6f4 v[66:69], v[226:233], v[180:187], v[66:69], v210, v210 op_sel_hi:[0,0,0]
	v_mfma_scale_f32_16x16x128_f8f6f4 v[54:57], v[234:241], v[180:187], v[54:57], v210, v210 op_sel_hi:[0,0,0]
	v_mfma_scale_f32_16x16x128_f8f6f4 v[42:45], v[226:233], v[188:195], v[42:45], v210, v210 op_sel_hi:[0,0,0]
	v_mfma_scale_f32_16x16x128_f8f6f4 v[34:37], v[234:241], v[188:195], v[34:37], v210, v210 op_sel_hi:[0,0,0]
	v_mfma_scale_f32_16x16x128_f8f6f4 v[26:29], v[226:233], v[196:203], v[26:29], v210, v210 op_sel_hi:[0,0,0]
	v_mfma_scale_f32_16x16x128_f8f6f4 v[18:21], v[234:241], v[196:203], v[18:21], v210, v210 op_sel_hi:[0,0,0]
	v_mfma_scale_f32_16x16x128_f8f6f4 v[10:13], v[226:233], v[218:225], v[10:13], v210, v210 op_sel_hi:[0,0,0]
	v_mfma_scale_f32_16x16x128_f8f6f4 v[2:5], v[234:241], v[218:225], v[2:5], v210, v210 op_sel_hi:[0,0,0]
	s_setprio 0
	s_barrier
	ds_read_b128 v[134:137], v142
	ds_read_b128 v[138:141], v142 offset:1024
	ds_read_b128 v[164:167], v142 offset:2048
	ds_read_b128 v[168:171], v142 offset:3072
	s_mov_b32 m0, s61
	v_lshl_add_u64 v[130:131], v[130:131], 0, s[58:59]
	ds_read_b128 v[172:175], v217
	ds_read_b128 v[176:179], v217 offset:1024
	ds_read_b128 v[180:183], v217 offset:2048
	ds_read_b128 v[184:187], v217 offset:3072
	ds_read_b128 v[188:191], v217 offset:4096
	ds_read_b128 v[192:195], v217 offset:5120
	ds_read_b128 v[196:199], v217 offset:6144
	ds_read_b128 v[200:203], v217 offset:7168
	global_load_lds_dwordx4 v[130:131], off
	v_lshl_add_u64 v[130:131], v[132:133], 0, s[58:59]
	s_mov_b32 m0, s13
	s_nop 0
	global_load_lds_dwordx4 v[130:131], off
	s_waitcnt lgkmcnt(8)
	s_barrier
	s_waitcnt lgkmcnt(0)
	s_setprio 1
	s_waitcnt lgkmcnt(0)
	v_mfma_scale_f32_16x16x128_f8f6f4 v[118:121], v[134:141], v[172:179], v[118:121], v210, v210 op_sel_hi:[0,0,0]
	v_mfma_scale_f32_16x16x128_f8f6f4 v[114:117], v[164:171], v[172:179], v[114:117], v210, v210 op_sel_hi:[0,0,0]
	v_mfma_scale_f32_16x16x128_f8f6f4 v[102:105], v[134:141], v[180:187], v[102:105], v210, v210 op_sel_hi:[0,0,0]
	v_mfma_scale_f32_16x16x128_f8f6f4 v[98:101], v[164:171], v[180:187], v[98:101], v210, v210 op_sel_hi:[0,0,0]
	v_mfma_scale_f32_16x16x128_f8f6f4 v[86:89], v[134:141], v[188:195], v[86:89], v210, v210 op_sel_hi:[0,0,0]
	v_mfma_scale_f32_16x16x128_f8f6f4 v[82:85], v[164:171], v[188:195], v[82:85], v210, v210 op_sel_hi:[0,0,0]
	v_mfma_scale_f32_16x16x128_f8f6f4 v[58:61], v[134:141], v[196:203], v[58:61], v210, v210 op_sel_hi:[0,0,0]
	v_mfma_scale_f32_16x16x128_f8f6f4 v[50:53], v[164:171], v[196:203], v[50:53], v210, v210 op_sel_hi:[0,0,0]
	s_setprio 0
	s_barrier
	s_mov_b32 m0, s41
	v_lshl_add_u64 v[160:161], s[26:27], 0, v[146:147]
	ds_read_b128 v[218:221], v143
	ds_read_b128 v[222:225], v143 offset:1024
	ds_read_b128 v[226:229], v143 offset:2048
	ds_read_b128 v[230:233], v143 offset:3072
	global_load_lds_dwordx4 v[160:161], off
	v_lshl_add_u64 v[204:205], s[26:27], 0, v[148:149]
	s_mov_b32 m0, s23
	s_nop 0
	global_load_lds_dwordx4 v[204:205], off
	s_barrier
	s_waitcnt lgkmcnt(0)
	s_setprio 1
	s_waitcnt lgkmcnt(0)
	v_mfma_scale_f32_16x16x128_f8f6f4 v[126:129], v[218:225], v[172:179], v[126:129], v210, v210 op_sel_hi:[0,0,0]
	v_mfma_scale_f32_16x16x128_f8f6f4 v[122:125], v[226:233], v[172:179], v[122:125], v210, v210 op_sel_hi:[0,0,0]
	v_mfma_scale_f32_16x16x128_f8f6f4 v[110:113], v[218:225], v[180:187], v[110:113], v210, v210 op_sel_hi:[0,0,0]
	v_mfma_scale_f32_16x16x128_f8f6f4 v[106:109], v[226:233], v[180:187], v[106:109], v210, v210 op_sel_hi:[0,0,0]
	v_mfma_scale_f32_16x16x128_f8f6f4 v[94:97], v[218:225], v[188:195], v[94:97], v210, v210 op_sel_hi:[0,0,0]
	v_mfma_scale_f32_16x16x128_f8f6f4 v[90:93], v[226:233], v[188:195], v[90:93], v210, v210 op_sel_hi:[0,0,0]
	v_mfma_scale_f32_16x16x128_f8f6f4 v[78:81], v[218:225], v[196:203], v[78:81], v210, v210 op_sel_hi:[0,0,0]
	v_mfma_scale_f32_16x16x128_f8f6f4 v[74:77], v[226:233], v[196:203], v[74:77], v210, v210 op_sel_hi:[0,0,0]
	s_setprio 0
	s_mov_b32 m0, s15
	v_lshl_add_u64 v[206:207], s[28:29], 0, v[150:151]
	s_barrier
	ds_read_b128 v[172:175], v217 offset:16384
	ds_read_b128 v[176:179], v217 offset:17408
	ds_read_b128 v[180:183], v217 offset:18432
	ds_read_b128 v[184:187], v217 offset:19456
	ds_read_b128 v[188:191], v217 offset:20480
	ds_read_b128 v[192:195], v217 offset:21504
	ds_read_b128 v[196:199], v217 offset:22528
	ds_read_b128 v[200:203], v217 offset:23552
	global_load_lds_dwordx4 v[206:207], off
	v_lshl_add_u64 v[208:209], s[28:29], 0, v[152:153]
	s_mov_b32 m0, s8
	s_nop 0
	global_load_lds_dwordx4 v[208:209], off
	s_barrier
	s_waitcnt lgkmcnt(0)
	s_setprio 1
	s_waitcnt lgkmcnt(0)
	v_mfma_scale_f32_16x16x128_f8f6f4 v[70:73], v[134:141], v[172:179], v[70:73], v210, v210 op_sel_hi:[0,0,0]
	v_mfma_scale_f32_16x16x128_f8f6f4 v[62:65], v[164:171], v[172:179], v[62:65], v210, v210 op_sel_hi:[0,0,0]
	v_mfma_scale_f32_16x16x128_f8f6f4 v[46:49], v[134:141], v[180:187], v[46:49], v210, v210 op_sel_hi:[0,0,0]
	v_mfma_scale_f32_16x16x128_f8f6f4 v[38:41], v[164:171], v[180:187], v[38:41], v210, v210 op_sel_hi:[0,0,0]
	v_mfma_scale_f32_16x16x128_f8f6f4 v[30:33], v[134:141], v[188:195], v[30:33], v210, v210 op_sel_hi:[0,0,0]
	v_mfma_scale_f32_16x16x128_f8f6f4 v[22:25], v[164:171], v[188:195], v[22:25], v210, v210 op_sel_hi:[0,0,0]
	v_mfma_scale_f32_16x16x128_f8f6f4 v[14:17], v[134:141], v[196:203], v[14:17], v210, v210 op_sel_hi:[0,0,0]
	v_mfma_scale_f32_16x16x128_f8f6f4 v[6:9], v[164:171], v[196:203], v[6:9], v210, v210 op_sel_hi:[0,0,0]
	s_setprio 0
	s_barrier
	s_add_u32 s90, s26, 0x10000
	s_addc_u32 s91, s27, 0
	s_mov_b32 m0, s19
	v_lshl_add_u64 v[130:131], s[90:91], 0, v[146:147]
	global_load_lds_dwordx4 v[130:131], off
	v_lshl_add_u64 v[130:131], s[90:91], 0, v[148:149]
	s_mov_b32 m0, s18
	s_nop 0
	global_load_lds_dwordx4 v[130:131], off
	s_waitcnt vmcnt(6)
	s_barrier
	s_setprio 1
	v_mfma_scale_f32_16x16x128_f8f6f4 v[66:69], v[218:225], v[172:179], v[66:69], v210, v210 op_sel_hi:[0,0,0]
	v_mfma_scale_f32_16x16x128_f8f6f4 v[54:57], v[226:233], v[172:179], v[54:57], v210, v210 op_sel_hi:[0,0,0]
	v_mfma_scale_f32_16x16x128_f8f6f4 v[42:45], v[218:225], v[180:187], v[42:45], v210, v210 op_sel_hi:[0,0,0]
	v_mfma_scale_f32_16x16x128_f8f6f4 v[34:37], v[226:233], v[180:187], v[34:37], v210, v210 op_sel_hi:[0,0,0]
	v_mfma_scale_f32_16x16x128_f8f6f4 v[26:29], v[218:225], v[188:195], v[26:29], v210, v210 op_sel_hi:[0,0,0]
	v_mfma_scale_f32_16x16x128_f8f6f4 v[18:21], v[226:233], v[188:195], v[18:21], v210, v210 op_sel_hi:[0,0,0]
	v_mfma_scale_f32_16x16x128_f8f6f4 v[10:13], v[218:225], v[196:203], v[10:13], v210, v210 op_sel_hi:[0,0,0]
	v_mfma_scale_f32_16x16x128_f8f6f4 v[2:5], v[226:233], v[196:203], v[2:5], v210, v210 op_sel_hi:[0,0,0]
	s_setprio 0
	s_barrier
	ds_read_b128 v[130:133], v144
	ds_read_b128 v[134:137], v144 offset:1024
	ds_read_b128 v[164:167], v144 offset:2048
	ds_read_b128 v[168:171], v144 offset:3072
	s_mov_b32 m0, s9
	v_lshl_add_u64 v[138:139], s[28:29], 0, v[154:155]
	ds_read_b128 v[172:175], v217 offset:32768
	ds_read_b128 v[176:179], v217 offset:33792
	ds_read_b128 v[180:183], v217 offset:34816
	ds_read_b128 v[184:187], v217 offset:35840
	ds_read_b128 v[188:191], v217 offset:36864
	ds_read_b128 v[192:195], v217 offset:37888
	ds_read_b128 v[196:199], v217 offset:38912
	ds_read_b128 v[200:203], v217 offset:39936
	global_load_lds_dwordx4 v[138:139], off
	v_lshl_add_u64 v[138:139], s[28:29], 0, v[156:157]
	s_mov_b32 m0, s82
	s_nop 0
	global_load_lds_dwordx4 v[138:139], off
	s_waitcnt lgkmcnt(8)
	s_barrier
	s_waitcnt lgkmcnt(0)
	s_setprio 1
	s_waitcnt lgkmcnt(0)
	v_mfma_scale_f32_16x16x128_f8f6f4 v[118:121], v[130:137], v[172:179], v[118:121], v210, v210 op_sel_hi:[0,0,0]
	v_mfma_scale_f32_16x16x128_f8f6f4 v[114:117], v[164:171], v[172:179], v[114:117], v210, v210 op_sel_hi:[0,0,0]
	v_mfma_scale_f32_16x16x128_f8f6f4 v[102:105], v[130:137], v[180:187], v[102:105], v210, v210 op_sel_hi:[0,0,0]
	v_mfma_scale_f32_16x16x128_f8f6f4 v[98:101], v[164:171], v[180:187], v[98:101], v210, v210 op_sel_hi:[0,0,0]
	v_mfma_scale_f32_16x16x128_f8f6f4 v[86:89], v[130:137], v[188:195], v[86:89], v210, v210 op_sel_hi:[0,0,0]
	v_mfma_scale_f32_16x16x128_f8f6f4 v[82:85], v[164:171], v[188:195], v[82:85], v210, v210 op_sel_hi:[0,0,0]
	v_mfma_scale_f32_16x16x128_f8f6f4 v[58:61], v[130:137], v[196:203], v[58:61], v210, v210 op_sel_hi:[0,0,0]
	v_mfma_scale_f32_16x16x128_f8f6f4 v[50:53], v[164:171], v[196:203], v[50:53], v210, v210 op_sel_hi:[0,0,0]
	s_setprio 0
	s_barrier
	s_mov_b32 m0, s42
	v_lshl_add_u64 v[160:161], v[160:161], 0, s[44:45]
	ds_read_b128 v[218:221], v145
	ds_read_b128 v[222:225], v145 offset:1024
	ds_read_b128 v[138:141], v145 offset:2048
	ds_read_b128 v[142:145], v145 offset:3072
	global_load_lds_dwordx4 v[160:161], off
	v_lshl_add_u64 v[160:161], v[204:205], 0, s[44:45]
	s_mov_b32 m0, s25
	s_nop 0
	global_load_lds_dwordx4 v[160:161], off
	s_barrier
	s_waitcnt lgkmcnt(0)
	s_setprio 1
	s_waitcnt lgkmcnt(0)
	v_mfma_scale_f32_16x16x128_f8f6f4 v[126:129], v[218:225], v[172:179], v[126:129], v210, v210 op_sel_hi:[0,0,0]
	v_mfma_scale_f32_16x16x128_f8f6f4 v[122:125], v[138:145], v[172:179], v[122:125], v210, v210 op_sel_hi:[0,0,0]
	v_mfma_scale_f32_16x16x128_f8f6f4 v[110:113], v[218:225], v[180:187], v[110:113], v210, v210 op_sel_hi:[0,0,0]
	v_mfma_scale_f32_16x16x128_f8f6f4 v[106:109], v[138:145], v[180:187], v[106:109], v210, v210 op_sel_hi:[0,0,0]
	v_mfma_scale_f32_16x16x128_f8f6f4 v[94:97], v[218:225], v[188:195], v[94:97], v210, v210 op_sel_hi:[0,0,0]
	v_mfma_scale_f32_16x16x128_f8f6f4 v[90:93], v[138:145], v[188:195], v[90:93], v210, v210 op_sel_hi:[0,0,0]
	v_mfma_scale_f32_16x16x128_f8f6f4 v[78:81], v[218:225], v[196:203], v[78:81], v210, v210 op_sel_hi:[0,0,0]
	v_mfma_scale_f32_16x16x128_f8f6f4 v[74:77], v[138:145], v[196:203], v[74:77], v210, v210 op_sel_hi:[0,0,0]
	s_setprio 0
	s_mov_b32 m0, s83
	v_lshl_add_u64 v[160:161], v[206:207], 0, s[44:45]
	s_barrier
	ds_read_b128 v[172:175], v217 offset:49152
	ds_read_b128 v[176:179], v217 offset:50176
	ds_read_b128 v[180:183], v217 offset:51200
	ds_read_b128 v[184:187], v217 offset:52224
	ds_read_b128 v[188:191], v217 offset:53248
	ds_read_b128 v[192:195], v217 offset:54272
	ds_read_b128 v[196:199], v217 offset:55296
	ds_read_b128 v[200:203], v217 offset:56320
	global_load_lds_dwordx4 v[160:161], off
	v_lshl_add_u64 v[160:161], v[208:209], 0, s[44:45]
	s_mov_b32 m0, s5
	s_nop 0
	global_load_lds_dwordx4 v[160:161], off
	s_barrier
	s_waitcnt lgkmcnt(0)
	s_setprio 1
	s_waitcnt lgkmcnt(0)
	v_mfma_scale_f32_16x16x128_f8f6f4 v[70:73], v[130:137], v[172:179], v[70:73], v210, v210 op_sel_hi:[0,0,0]
	v_mfma_scale_f32_16x16x128_f8f6f4 v[62:65], v[164:171], v[172:179], v[62:65], v210, v210 op_sel_hi:[0,0,0]
	v_mfma_scale_f32_16x16x128_f8f6f4 v[46:49], v[130:137], v[180:187], v[46:49], v210, v210 op_sel_hi:[0,0,0]
	v_mfma_scale_f32_16x16x128_f8f6f4 v[38:41], v[164:171], v[180:187], v[38:41], v210, v210 op_sel_hi:[0,0,0]
	v_mfma_scale_f32_16x16x128_f8f6f4 v[30:33], v[130:137], v[188:195], v[30:33], v210, v210 op_sel_hi:[0,0,0]
	v_mfma_scale_f32_16x16x128_f8f6f4 v[22:25], v[164:171], v[188:195], v[22:25], v210, v210 op_sel_hi:[0,0,0]
	v_mfma_scale_f32_16x16x128_f8f6f4 v[14:17], v[130:137], v[196:203], v[14:17], v210, v210 op_sel_hi:[0,0,0]
	v_mfma_scale_f32_16x16x128_f8f6f4 v[6:9], v[164:171], v[196:203], v[6:9], v210, v210 op_sel_hi:[0,0,0]
	s_setprio 0
	s_barrier
	s_add_u32 s18, s26, 0x10080
	s_addc_u32 s19, s27, 0
	s_mov_b32 m0, s21
	v_lshl_add_u64 v[130:131], s[18:19], 0, v[146:147]
	global_load_lds_dwordx4 v[130:131], off
	v_lshl_add_u64 v[130:131], s[18:19], 0, v[148:149]
	s_mov_b32 m0, s20
	s_nop 0
	global_load_lds_dwordx4 v[130:131], off
	s_waitcnt vmcnt(6)
	s_barrier
	s_setprio 1
	v_mfma_scale_f32_16x16x128_f8f6f4 v[66:69], v[218:225], v[172:179], v[66:69], v210, v210 op_sel_hi:[0,0,0]
	v_mfma_scale_f32_16x16x128_f8f6f4 v[54:57], v[138:145], v[172:179], v[54:57], v210, v210 op_sel_hi:[0,0,0]
	v_mfma_scale_f32_16x16x128_f8f6f4 v[42:45], v[218:225], v[180:187], v[42:45], v210, v210 op_sel_hi:[0,0,0]
	v_mfma_scale_f32_16x16x128_f8f6f4 v[34:37], v[138:145], v[180:187], v[34:37], v210, v210 op_sel_hi:[0,0,0]
	v_mfma_scale_f32_16x16x128_f8f6f4 v[26:29], v[218:225], v[188:195], v[26:29], v210, v210 op_sel_hi:[0,0,0]
	v_mfma_scale_f32_16x16x128_f8f6f4 v[18:21], v[138:145], v[188:195], v[18:21], v210, v210 op_sel_hi:[0,0,0]
	v_mfma_scale_f32_16x16x128_f8f6f4 v[10:13], v[218:225], v[196:203], v[10:13], v210, v210 op_sel_hi:[0,0,0]
	v_mfma_scale_f32_16x16x128_f8f6f4 v[2:5], v[138:145], v[196:203], v[2:5], v210, v210 op_sel_hi:[0,0,0]
	s_setprio 0
	v_lshlrev_b32_e32 v130, 3, v214
	v_add_u32_e32 v130, 0x20000, v130
	s_barrier
	s_nop 15
	s_nop 15
	ds_read_b64 v[176:177], v130
	ds_read_b64 v[174:175], v130 offset:128
	ds_read_b64 v[172:173], v130 offset:256
	ds_read_b64 v[170:171], v130 offset:384
	ds_read_b64 v[168:169], v130 offset:1024
	ds_read_b64 v[166:167], v130 offset:1152
	ds_read_b64 v[164:165], v130 offset:1280
	ds_read_b64 v[160:161], v130 offset:1408
	s_cmp_lt_i32 s12, 64
	s_cbranch_scc1 .LBB0_3627
	s_waitcnt lgkmcnt(0)
	v_ashrrev_i32_e32 v130, 13, v177
	v_mul_i32_i24_e32 v130, 0x3000, v130
	v_lshl_or_b32 v186, s51, 8, v216
	v_ashrrev_i32_e32 v131, 31, v130
	v_ashrrev_i32_e32 v187, 31, v186
	v_lshl_add_u64 v[130:131], v[130:131], 2, s[46:47]
	s_mov_b64 s[12:13], 0xf000
	v_lshlrev_b64 v[178:179], 1, v[186:187]
	v_ashrrev_i32_e32 v139, 31, v177
	v_mov_b32_e32 v138, v177
	v_lshl_add_u64 v[188:189], v[130:131], 0, s[12:13]
	v_lshl_add_u64 v[180:181], s[6:7], 0, v[178:179]
	v_lshlrev_b64 v[190:191], 12, v[138:139]
	v_lshl_add_u64 v[182:183], v[186:187], 2, v[188:189]
	v_lshl_add_u64 v[138:139], v[180:181], 0, v[190:191]
	global_load_dwordx4 v[130:133], v[182:183], off offset:16
	global_load_dwordx4 v[134:137], v[182:183], off
	global_load_dwordx4 v[196:199], v[138:139], off
	v_ashrrev_i32_e32 v139, 31, v175
	v_mov_b32_e32 v138, v175
	v_lshlrev_b64 v[184:185], 12, v[138:139]
	v_lshl_add_u64 v[138:139], v[180:181], 0, v[184:185]
	global_load_dwordx4 v[206:209], v[138:139], off
	v_ashrrev_i32_e32 v139, 31, v173
	v_mov_b32_e32 v138, v173
	v_lshlrev_b64 v[192:193], 12, v[138:139]
	v_lshl_add_u64 v[138:139], v[180:181], 0, v[192:193]
	global_load_dwordx4 v[142:145], v[138:139], off
	v_ashrrev_i32_e32 v139, 31, v171
	v_mov_b32_e32 v138, v171
	v_lshlrev_b64 v[194:195], 12, v[138:139]
	v_lshl_add_u64 v[138:139], v[180:181], 0, v[194:195]
	global_load_dwordx4 v[138:141], v[138:139], off
	v_mov_b32_e32 v200, v118
	v_mov_b32_e32 v218, v114
	v_mov_b32_e32 v202, v119
	v_mov_b32_e32 v220, v115
	v_mov_b32_e32 v204, v120
	v_mov_b32_e32 v222, v116
	s_mov_b64 vcc, 0
	s_waitcnt vmcnt(0)
	v_lshlrev_b32_e32 v201, 16, v196
	v_and_b32_e32 v203, 0xffff0000, v196
	v_lshlrev_b32_e32 v205, 16, v197
	v_and_b32_e32 v197, 0xffff0000, v197
	v_lshlrev_b32_e32 v219, 16, v198
	v_and_b32_e32 v221, 0xffff0000, v198
	v_lshlrev_b32_e32 v223, 16, v199
	v_and_b32_e32 v199, 0xffff0000, v199
	v_pk_mul_f32 v[200:201], v[200:201], s[56:57]
	v_mov_b32_e32 v196, v121
	v_mov_b32_e32 v198, v117
	v_fmac_f32_e32 v201, v200, v134
	v_pk_mul_f32 v[218:219], v[218:219], s[56:57]
	v_pk_mul_f32 v[202:203], v[202:203], s[56:57]
	v_pk_mul_f32 v[220:221], v[220:221], s[56:57]
	v_pk_mul_f32 v[204:205], v[204:205], s[56:57]
	v_pk_mul_f32 v[222:223], v[222:223], s[56:57]
	v_pk_mul_f32 v[224:225], v[196:197], s[56:57]
	v_pk_mul_f32 v[226:227], v[198:199], s[56:57]
	v_lshl_add_u64 v[196:197], s[62:63], 0, v[190:191]
	v_fmac_f32_e32 v219, v218, v130
	v_fmac_f32_e32 v203, v202, v135
	v_fmac_f32_e32 v221, v220, v131
	v_fmac_f32_e32 v205, v204, v136
	v_fmac_f32_e32 v223, v222, v132
	v_fmac_f32_e32 v225, v224, v137
	v_fmac_f32_e32 v227, v226, v133
	v_lshl_add_u64 v[196:197], v[196:197], 0, v[178:179]
	v_cvt_pk_bf16_f32 v198, v201, v203
	v_cvt_pk_bf16_f32 v199, v205, v225
	v_cvt_pk_bf16_f32 v200, v219, v221
	v_cvt_pk_bf16_f32 v201, v223, v227
	global_store_dwordx4 v[196:197], v[198:201], off
	v_lshlrev_b32_e32 v219, 16, v206
	v_and_b32_e32 v221, 0xffff0000, v206
	v_and_b32_e32 v201, 0xffff0000, v207
	v_mov_b32_e32 v200, v105
	v_lshlrev_b32_e32 v205, 16, v207
	v_lshlrev_b32_e32 v223, 16, v208
	v_lshlrev_b32_e32 v203, 16, v209
	v_and_b32_e32 v199, 0xffff0000, v209
	v_mov_b32_e32 v218, v102
	v_mov_b32_e32 v222, v98
	v_mov_b32_e32 v220, v103
	v_mov_b32_e32 v204, v104
	v_mov_b32_e32 v202, v100
	v_pk_mul_f32 v[200:201], v[200:201], s[56:57]
	v_mov_b32_e32 v198, v101
	v_and_b32_e32 v207, 0xffff0000, v208
	v_pk_mul_f32 v[208:209], v[218:219], s[56:57]
	v_pk_mul_f32 v[218:219], v[222:223], s[56:57]
	v_pk_mul_f32 v[220:221], v[220:221], s[56:57]
	v_mov_b32_e32 v206, v99
	v_pk_mul_f32 v[204:205], v[204:205], s[56:57]
	v_pk_mul_f32 v[202:203], v[202:203], s[56:57]
	v_fmac_f32_e32 v201, v200, v137
	v_pk_mul_f32 v[222:223], v[198:199], s[56:57]
	v_lshl_add_u64 v[198:199], s[62:63], 0, v[184:185]
	v_fmac_f32_e32 v209, v208, v134
	v_fmac_f32_e32 v221, v220, v135
	v_pk_mul_f32 v[206:207], v[206:207], s[56:57]
	v_fmac_f32_e32 v205, v204, v136
	v_fmac_f32_e32 v203, v202, v132
	v_lshl_add_u64 v[198:199], v[198:199], 0, v[178:179]
	v_cvt_pk_bf16_f32 v200, v209, v221
	v_cvt_pk_bf16_f32 v201, v205, v201
	v_fmac_f32_e32 v219, v218, v130
	v_fmac_f32_e32 v207, v206, v131
	v_fmac_f32_e32 v223, v222, v133
	v_cvt_pk_bf16_f32 v202, v219, v207
	v_cvt_pk_bf16_f32 v203, v203, v223
	global_store_dwordx4 v[198:199], v[200:203], off
	v_lshlrev_b32_e32 v205, 16, v143
	v_and_b32_e32 v143, 0xffff0000, v143
	v_lshlrev_b32_e32 v201, 16, v142
	v_mov_b32_e32 v200, v86
	v_and_b32_e32 v203, 0xffff0000, v142
	v_lshlrev_b32_e32 v207, 16, v144
	v_and_b32_e32 v209, 0xffff0000, v144
	v_lshlrev_b32_e32 v219, 16, v145
	v_and_b32_e32 v145, 0xffff0000, v145
	v_pk_mul_f32 v[200:201], v[200:201], s[56:57]
	v_mov_b32_e32 v202, v87
	v_mov_b32_e32 v204, v88
	v_mov_b32_e32 v142, v89
	v_mov_b32_e32 v144, v85
	v_fmac_f32_e32 v201, v200, v134
	v_mov_b32_e32 v206, v82
	v_pk_mul_f32 v[202:203], v[202:203], s[56:57]
	v_mov_b32_e32 v208, v83
	v_pk_mul_f32 v[204:205], v[204:205], s[56:57]
	v_mov_b32_e32 v218, v84
	v_pk_mul_f32 v[220:221], v[142:143], s[56:57]
	v_pk_mul_f32 v[144:145], v[144:145], s[56:57]
	v_lshl_add_u64 v[142:143], s[62:63], 0, v[192:193]
	v_pk_mul_f32 v[206:207], v[206:207], s[56:57]
	v_fmac_f32_e32 v203, v202, v135
	v_pk_mul_f32 v[208:209], v[208:209], s[56:57]
	v_fmac_f32_e32 v205, v204, v136
	v_pk_mul_f32 v[218:219], v[218:219], s[56:57]
	v_fmac_f32_e32 v221, v220, v137
	v_fmac_f32_e32 v145, v144, v133
	v_lshl_add_u64 v[142:143], v[142:143], 0, v[178:179]
	v_cvt_pk_bf16_f32 v200, v201, v203
	v_cvt_pk_bf16_f32 v201, v205, v221
	v_fmac_f32_e32 v207, v206, v130
	v_fmac_f32_e32 v209, v208, v131
	v_fmac_f32_e32 v219, v218, v132
	v_cvt_pk_bf16_f32 v202, v207, v209
	v_cvt_pk_bf16_f32 v203, v219, v145
	global_store_dwordx4 v[142:143], v[200:203], off
	v_lshlrev_b32_e32 v145, 16, v138
	v_mov_b32_e32 v144, v58
	v_and_b32_e32 v201, 0xffff0000, v138
	v_mov_b32_e32 v200, v59
	v_lshlrev_b32_e32 v205, 16, v140
	v_and_b32_e32 v207, 0xffff0000, v140
	v_pk_mul_f32 v[218:219], v[144:145], s[56:57]
	v_mov_b32_e32 v204, v50
	v_pk_mul_f32 v[200:201], v[200:201], s[56:57]
	v_mov_b32_e32 v206, v51
	v_lshlrev_b32_e32 v203, 16, v139
	v_and_b32_e32 v139, 0xffff0000, v139
	v_fmac_f32_e32 v219, v218, v134
	v_pk_mul_f32 v[204:205], v[204:205], s[56:57]
	v_fmac_f32_e32 v201, v200, v135
	v_pk_mul_f32 v[134:135], v[206:207], s[56:57]
	v_mov_b32_e32 v202, v60
	v_mov_b32_e32 v138, v61
	v_lshlrev_b32_e32 v209, 16, v141
	v_and_b32_e32 v141, 0xffff0000, v141
	v_fmac_f32_e32 v205, v204, v130
	v_fmac_f32_e32 v135, v134, v131
	v_pk_mul_f32 v[130:131], v[202:203], s[56:57]
	v_mov_b32_e32 v208, v52
	v_pk_mul_f32 v[138:139], v[138:139], s[56:57]
	v_mov_b32_e32 v140, v53
	v_fmac_f32_e32 v131, v130, v136
	v_pk_mul_f32 v[202:203], v[208:209], s[56:57]
	v_fmac_f32_e32 v139, v138, v137
	v_pk_mul_f32 v[136:137], v[140:141], s[56:57]
	v_or_b32_e32 v138, 0x80, v186
	v_fmac_f32_e32 v203, v202, v132
	v_fmac_f32_e32 v137, v136, v133
	v_lshl_add_u64 v[132:133], s[62:63], 0, v[194:195]
	v_cvt_pk_bf16_f32 v130, v219, v201
	v_cvt_pk_bf16_f32 v131, v131, v139
	v_ashrrev_i32_e32 v139, 31, v138
	v_lshl_add_u64 v[144:145], v[132:133], 0, v[178:179]
	v_lshl_add_u64 v[140:141], v[138:139], 2, v[188:189]
	v_lshl_add_u64 v[186:187], s[6:7], 0, v[190:191]
	v_lshlrev_b64 v[138:139], 1, v[138:139]
	v_cvt_pk_bf16_f32 v132, v205, v135
	v_cvt_pk_bf16_f32 v133, v203, v137
	global_store_dwordx4 v[144:145], v[130:133], off
	v_lshl_add_u64 v[186:187], v[186:187], 0, v[138:139]
	global_load_dwordx4 v[130:133], v[140:141], off offset:16
	global_load_dwordx4 v[134:137], v[140:141], off
	v_lshl_add_u64 v[184:185], s[6:7], 0, v[184:185]
	global_load_dwordx4 v[186:189], v[186:187], off
	v_lshl_add_u64 v[184:185], v[184:185], 0, v[138:139]
	global_load_dwordx4 v[200:203], v[184:185], off
	v_lshl_add_u64 v[184:185], s[6:7], 0, v[192:193]
	v_lshl_add_u64 v[184:185], v[184:185], 0, v[138:139]
	global_load_dwordx4 v[190:193], v[184:185], off
	v_lshl_add_u64 v[184:185], s[6:7], 0, v[194:195]
	v_lshl_add_u64 v[184:185], v[184:185], 0, v[138:139]
	global_load_dwordx4 v[204:207], v[184:185], off
	v_mov_b32_e32 v184, v126
	v_mov_b32_e32 v194, v127
	v_mov_b32_e32 v208, v128
	v_mov_b32_e32 v218, v122
	v_mov_b32_e32 v220, v123
	v_mov_b32_e32 v222, v124
	s_waitcnt vmcnt(0)
	v_lshlrev_b32_e32 v185, 16, v186
	v_and_b32_e32 v195, 0xffff0000, v186
	v_lshlrev_b32_e32 v209, 16, v187
	v_and_b32_e32 v187, 0xffff0000, v187
	v_pk_mul_f32 v[184:185], v[184:185], s[56:57]
	v_mov_b32_e32 v186, v129
	v_lshlrev_b32_e32 v219, 16, v188
	v_and_b32_e32 v221, 0xffff0000, v188
	v_lshlrev_b32_e32 v223, 16, v189
	v_and_b32_e32 v189, 0xffff0000, v189
	v_fmac_f32_e32 v185, v184, v134
	v_pk_mul_f32 v[194:195], v[194:195], s[56:57]
	v_pk_mul_f32 v[208:209], v[208:209], s[56:57]
	v_pk_mul_f32 v[186:187], v[186:187], s[56:57]
	v_mov_b32_e32 v188, v125
	v_pk_mul_f32 v[218:219], v[218:219], s[56:57]
	v_fmac_f32_e32 v195, v194, v135
	v_pk_mul_f32 v[220:221], v[220:221], s[56:57]
	v_fmac_f32_e32 v209, v208, v136
	v_pk_mul_f32 v[222:223], v[222:223], s[56:57]
	v_fmac_f32_e32 v187, v186, v137
	v_pk_mul_f32 v[188:189], v[188:189], s[56:57]
	v_cvt_pk_bf16_f32 v184, v185, v195
	v_cvt_pk_bf16_f32 v185, v209, v187
	v_fmac_f32_e32 v219, v218, v130
	v_fmac_f32_e32 v221, v220, v131
	v_fmac_f32_e32 v223, v222, v132
	v_fmac_f32_e32 v189, v188, v133
	v_cvt_pk_bf16_f32 v186, v219, v221
	v_cvt_pk_bf16_f32 v187, v223, v189
	global_store_dwordx4 v[196:197], v[184:187], off offset:256
	v_lshlrev_b32_e32 v189, 16, v201
	v_and_b32_e32 v195, 0xffff0000, v201
	v_lshlrev_b32_e32 v185, 16, v200
	v_mov_b32_e32 v184, v110
	v_and_b32_e32 v187, 0xffff0000, v200
	v_pk_mul_f32 v[184:185], v[184:185], s[56:57]
	v_mov_b32_e32 v186, v111
	v_mov_b32_e32 v188, v112
	v_mov_b32_e32 v194, v113
	v_lshlrev_b32_e32 v197, 16, v202
	v_and_b32_e32 v201, 0xffff0000, v202
	v_lshlrev_b32_e32 v209, 16, v203
	v_and_b32_e32 v203, 0xffff0000, v203
	v_fmac_f32_e32 v185, v184, v134
	v_mov_b32_e32 v196, v106
	v_pk_mul_f32 v[186:187], v[186:187], s[56:57]
	v_mov_b32_e32 v200, v107
	v_pk_mul_f32 v[188:189], v[188:189], s[56:57]
	v_mov_b32_e32 v208, v108
	v_pk_mul_f32 v[194:195], v[194:195], s[56:57]
	v_mov_b32_e32 v202, v109
	v_pk_mul_f32 v[196:197], v[196:197], s[56:57]
	v_fmac_f32_e32 v187, v186, v135
	v_pk_mul_f32 v[200:201], v[200:201], s[56:57]
	v_fmac_f32_e32 v189, v188, v136
	v_pk_mul_f32 v[208:209], v[208:209], s[56:57]
	v_fmac_f32_e32 v195, v194, v137
	v_pk_mul_f32 v[202:203], v[202:203], s[56:57]
	v_cvt_pk_bf16_f32 v184, v185, v187
	v_cvt_pk_bf16_f32 v185, v189, v195
	v_fmac_f32_e32 v197, v196, v130
	v_fmac_f32_e32 v201, v200, v131
	v_fmac_f32_e32 v209, v208, v132
	v_fmac_f32_e32 v203, v202, v133
	v_cvt_pk_bf16_f32 v186, v197, v201
	v_cvt_pk_bf16_f32 v187, v209, v203
	global_store_dwordx4 v[198:199], v[184:187], off offset:256
	v_lshlrev_b32_e32 v189, 16, v191
	v_and_b32_e32 v191, 0xffff0000, v191
	v_lshlrev_b32_e32 v185, 16, v190
	v_mov_b32_e32 v184, v94
	v_and_b32_e32 v187, 0xffff0000, v190
	v_pk_mul_f32 v[184:185], v[184:185], s[56:57]
	v_mov_b32_e32 v186, v95
	v_mov_b32_e32 v188, v96
	v_mov_b32_e32 v190, v97
	v_lshlrev_b32_e32 v195, 16, v192
	v_and_b32_e32 v197, 0xffff0000, v192
	v_lshlrev_b32_e32 v199, 16, v193
	v_and_b32_e32 v193, 0xffff0000, v193
	v_fmac_f32_e32 v185, v184, v134
	v_mov_b32_e32 v194, v90
	v_pk_mul_f32 v[186:187], v[186:187], s[56:57]
	v_mov_b32_e32 v196, v91
	v_pk_mul_f32 v[188:189], v[188:189], s[56:57]
	v_mov_b32_e32 v198, v92
	v_pk_mul_f32 v[190:191], v[190:191], s[56:57]
	v_mov_b32_e32 v192, v93
	v_pk_mul_f32 v[194:195], v[194:195], s[56:57]
	v_fmac_f32_e32 v187, v186, v135
	v_pk_mul_f32 v[196:197], v[196:197], s[56:57]
	v_fmac_f32_e32 v189, v188, v136
	v_pk_mul_f32 v[198:199], v[198:199], s[56:57]
	v_fmac_f32_e32 v191, v190, v137
	v_pk_mul_f32 v[192:193], v[192:193], s[56:57]
	v_cvt_pk_bf16_f32 v184, v185, v187
	v_cvt_pk_bf16_f32 v185, v189, v191
	v_fmac_f32_e32 v195, v194, v130
	v_fmac_f32_e32 v197, v196, v131
	v_fmac_f32_e32 v199, v198, v132
	v_fmac_f32_e32 v193, v192, v133
	v_cvt_pk_bf16_f32 v186, v195, v197
	v_cvt_pk_bf16_f32 v187, v199, v193
	global_store_dwordx4 v[142:143], v[184:187], off offset:256
	v_lshlrev_b32_e32 v143, 16, v204
	v_mov_b32_e32 v142, v78
	v_and_b32_e32 v185, 0xffff0000, v204
	v_mov_b32_e32 v184, v79
	v_lshlrev_b32_e32 v191, 16, v206
	v_and_b32_e32 v193, 0xffff0000, v206
	v_pk_mul_f32 v[142:143], v[142:143], s[56:57]
	v_mov_b32_e32 v190, v74
	v_pk_mul_f32 v[184:185], v[184:185], s[56:57]
	v_mov_b32_e32 v192, v75
	v_lshlrev_b32_e32 v187, 16, v205
	v_and_b32_e32 v189, 0xffff0000, v205
	v_fmac_f32_e32 v143, v142, v134
	v_pk_mul_f32 v[190:191], v[190:191], s[56:57]
	v_fmac_f32_e32 v185, v184, v135
	v_pk_mul_f32 v[134:135], v[192:193], s[56:57]
	v_mov_b32_e32 v186, v80
	v_mov_b32_e32 v188, v81
	v_lshlrev_b32_e32 v195, 16, v207
	v_and_b32_e32 v197, 0xffff0000, v207
	v_fmac_f32_e32 v191, v190, v130
	v_fmac_f32_e32 v135, v134, v131
	v_pk_mul_f32 v[130:131], v[186:187], s[56:57]
	v_mov_b32_e32 v194, v76
	v_pk_mul_f32 v[188:189], v[188:189], s[56:57]
	v_mov_b32_e32 v196, v77
	v_fmac_f32_e32 v131, v130, v136
	v_pk_mul_f32 v[186:187], v[194:195], s[56:57]
	v_fmac_f32_e32 v189, v188, v137
	v_pk_mul_f32 v[136:137], v[196:197], s[56:57]
	v_fmac_f32_e32 v187, v186, v132
	v_fmac_f32_e32 v137, v136, v133
	v_cvt_pk_bf16_f32 v130, v143, v185
	v_cvt_pk_bf16_f32 v131, v131, v189
	v_cvt_pk_bf16_f32 v132, v191, v135
	v_cvt_pk_bf16_f32 v133, v187, v137
	global_store_dwordx4 v[144:145], v[130:133], off offset:256
	v_ashrrev_i32_e32 v143, 31, v169
	v_mov_b32_e32 v142, v169
	global_load_dwordx4 v[130:133], v[182:183], off offset:16
	global_load_dwordx4 v[134:137], v[182:183], off
	v_lshlrev_b64 v[182:183], 12, v[142:143]
	v_lshl_add_u64 v[142:143], v[180:181], 0, v[182:183]
	global_load_dwordx4 v[188:191], v[142:143], off
	v_ashrrev_i32_e32 v143, 31, v167
	v_mov_b32_e32 v142, v167
	v_lshlrev_b64 v[142:143], 12, v[142:143]
	v_lshl_add_u64 v[144:145], v[180:181], 0, v[142:143]
	global_load_dwordx4 v[192:195], v[144:145], off
	v_ashrrev_i32_e32 v145, 31, v165
	v_mov_b32_e32 v144, v165
	v_lshlrev_b64 v[144:145], 12, v[144:145]
	v_lshl_add_u64 v[184:185], v[180:181], 0, v[144:145]
	global_load_dwordx4 v[196:199], v[184:185], off
	v_ashrrev_i32_e32 v185, 31, v161
	v_mov_b32_e32 v184, v161
	v_lshlrev_b64 v[186:187], 12, v[184:185]
	v_lshl_add_u64 v[180:181], v[180:181], 0, v[186:187]
	global_load_dwordx4 v[200:203], v[180:181], off
	v_mov_b32_e32 v180, v70
	v_mov_b32_e32 v206, v62
	v_mov_b32_e32 v184, v71
	v_mov_b32_e32 v208, v63
	v_mov_b32_e32 v204, v72
	v_mov_b32_e32 v218, v64
	s_waitcnt vmcnt(0)
	v_lshlrev_b32_e32 v181, 16, v188
	v_and_b32_e32 v185, 0xffff0000, v188
	v_lshlrev_b32_e32 v205, 16, v189
	v_and_b32_e32 v189, 0xffff0000, v189
	v_lshlrev_b32_e32 v207, 16, v190
	v_and_b32_e32 v209, 0xffff0000, v190
	v_lshlrev_b32_e32 v219, 16, v191
	v_and_b32_e32 v191, 0xffff0000, v191
	v_mov_b32_e32 v188, v73
	v_mov_b32_e32 v190, v65
	v_pk_mul_f32 v[188:189], v[188:189], s[56:57]
	v_pk_mul_f32 v[190:191], v[190:191], s[56:57]
	v_pk_mul_f32 v[220:221], v[180:181], s[56:57]
	v_pk_mul_f32 v[206:207], v[206:207], s[56:57]
	v_pk_mul_f32 v[184:185], v[184:185], s[56:57]
	v_pk_mul_f32 v[208:209], v[208:209], s[56:57]
	v_pk_mul_f32 v[204:205], v[204:205], s[56:57]
	v_pk_mul_f32 v[218:219], v[218:219], s[56:57]
	v_fmac_f32_e32 v189, v188, v137
	v_fmac_f32_e32 v191, v190, v133
	v_lshl_add_u64 v[180:181], s[62:63], 0, v[182:183]
	v_fmac_f32_e32 v221, v220, v134
	v_fmac_f32_e32 v207, v206, v130
	v_fmac_f32_e32 v185, v184, v135
	v_fmac_f32_e32 v209, v208, v131
	v_fmac_f32_e32 v205, v204, v136
	v_fmac_f32_e32 v219, v218, v132
	v_lshl_add_u64 v[180:181], v[180:181], 0, v[178:179]
	v_cvt_pk_bf16_f32 v188, v221, v185
	v_cvt_pk_bf16_f32 v189, v205, v189
	v_cvt_pk_bf16_f32 v190, v207, v209
	v_cvt_pk_bf16_f32 v191, v219, v191
	global_store_dwordx4 v[180:181], v[188:191], off
	v_lshlrev_b32_e32 v185, 16, v192
	v_lshlrev_b32_e32 v205, 16, v194
	v_and_b32_e32 v189, 0xffff0000, v192
	v_lshlrev_b32_e32 v191, 16, v193
	v_mov_b32_e32 v188, v47
	v_mov_b32_e32 v190, v48
	v_and_b32_e32 v193, 0xffff0000, v193
	v_and_b32_e32 v207, 0xffff0000, v194
	v_lshlrev_b32_e32 v209, 16, v195
	v_and_b32_e32 v195, 0xffff0000, v195
	v_mov_b32_e32 v184, v46
	v_mov_b32_e32 v204, v38
	v_pk_mul_f32 v[188:189], v[188:189], s[56:57]
	v_mov_b32_e32 v206, v39
	v_pk_mul_f32 v[190:191], v[190:191], s[56:57]
	v_mov_b32_e32 v208, v40
	v_mov_b32_e32 v192, v49
	v_mov_b32_e32 v194, v41
	v_pk_mul_f32 v[218:219], v[184:185], s[56:57]
	v_pk_mul_f32 v[204:205], v[204:205], s[56:57]
	v_fmac_f32_e32 v189, v188, v135
	v_pk_mul_f32 v[206:207], v[206:207], s[56:57]
	v_fmac_f32_e32 v191, v190, v136
	v_pk_mul_f32 v[208:209], v[208:209], s[56:57]
	v_pk_mul_f32 v[192:193], v[192:193], s[56:57]
	v_pk_mul_f32 v[194:195], v[194:195], s[56:57]
	v_lshl_add_u64 v[184:185], s[62:63], 0, v[142:143]
	v_fmac_f32_e32 v219, v218, v134
	v_fmac_f32_e32 v205, v204, v130
	v_fmac_f32_e32 v207, v206, v131
	v_fmac_f32_e32 v209, v208, v132
	v_fmac_f32_e32 v193, v192, v137
	v_fmac_f32_e32 v195, v194, v133
	v_lshl_add_u64 v[184:185], v[184:185], 0, v[178:179]
	v_cvt_pk_bf16_f32 v188, v219, v189
	v_cvt_pk_bf16_f32 v189, v191, v193
	v_cvt_pk_bf16_f32 v190, v205, v207
	v_cvt_pk_bf16_f32 v191, v209, v195
	global_store_dwordx4 v[184:185], v[188:191], off
	v_lshlrev_b32_e32 v193, 16, v197
	v_mov_b32_e32 v192, v32
	v_and_b32_e32 v191, 0xffff0000, v196
	v_mov_b32_e32 v190, v31
	v_lshlrev_b32_e32 v189, 16, v196
	v_and_b32_e32 v195, 0xffff0000, v197
	v_lshlrev_b32_e32 v197, 16, v198
	v_and_b32_e32 v205, 0xffff0000, v198
	v_lshlrev_b32_e32 v207, 16, v199
	v_and_b32_e32 v199, 0xffff0000, v199
	v_mov_b32_e32 v188, v30
	v_mov_b32_e32 v196, v22
	v_pk_mul_f32 v[190:191], v[190:191], s[56:57]
	v_mov_b32_e32 v204, v23
	v_pk_mul_f32 v[192:193], v[192:193], s[56:57]
	v_mov_b32_e32 v206, v24
	v_mov_b32_e32 v194, v33
	v_mov_b32_e32 v198, v25
	v_pk_mul_f32 v[208:209], v[188:189], s[56:57]
	v_pk_mul_f32 v[196:197], v[196:197], s[56:57]
	v_fmac_f32_e32 v191, v190, v135
	v_pk_mul_f32 v[204:205], v[204:205], s[56:57]
	v_fmac_f32_e32 v193, v192, v136
	v_pk_mul_f32 v[206:207], v[206:207], s[56:57]
	v_pk_mul_f32 v[194:195], v[194:195], s[56:57]
	v_pk_mul_f32 v[198:199], v[198:199], s[56:57]
	v_lshl_add_u64 v[188:189], s[62:63], 0, v[144:145]
	v_fmac_f32_e32 v209, v208, v134
	v_fmac_f32_e32 v197, v196, v130
	v_fmac_f32_e32 v205, v204, v131
	v_fmac_f32_e32 v207, v206, v132
	v_fmac_f32_e32 v195, v194, v137
	v_fmac_f32_e32 v199, v198, v133
	v_lshl_add_u64 v[188:189], v[188:189], 0, v[178:179]
	v_cvt_pk_bf16_f32 v190, v209, v191
	v_cvt_pk_bf16_f32 v191, v193, v195
	v_cvt_pk_bf16_f32 v192, v197, v205
	v_cvt_pk_bf16_f32 v193, v207, v199
	global_store_dwordx4 v[188:189], v[190:193], off
	v_lshlrev_b32_e32 v195, 16, v201
	v_and_b32_e32 v197, 0xffff0000, v201
	v_lshlrev_b32_e32 v191, 16, v200
	v_and_b32_e32 v193, 0xffff0000, v200
	v_mov_b32_e32 v190, v14
	v_mov_b32_e32 v192, v15
	v_lshlrev_b32_e32 v199, 16, v202
	v_and_b32_e32 v201, 0xffff0000, v202
	v_pk_mul_f32 v[190:191], v[190:191], s[56:57]
	v_mov_b32_e32 v198, v6
	v_pk_mul_f32 v[192:193], v[192:193], s[56:57]
	v_mov_b32_e32 v200, v7
	v_fmac_f32_e32 v191, v190, v134
	v_pk_mul_f32 v[198:199], v[198:199], s[56:57]
	v_fmac_f32_e32 v193, v192, v135
	v_pk_mul_f32 v[134:135], v[200:201], s[56:57]
	v_mov_b32_e32 v194, v16
	v_mov_b32_e32 v196, v17
	v_lshlrev_b32_e32 v205, 16, v203
	v_and_b32_e32 v203, 0xffff0000, v203
	v_fmac_f32_e32 v199, v198, v130
	v_fmac_f32_e32 v135, v134, v131
	v_pk_mul_f32 v[130:131], v[194:195], s[56:57]
	v_mov_b32_e32 v204, v8
	v_pk_mul_f32 v[196:197], v[196:197], s[56:57]
	v_mov_b32_e32 v202, v9
	v_fmac_f32_e32 v131, v130, v136
	v_pk_mul_f32 v[194:195], v[204:205], s[56:57]
	v_fmac_f32_e32 v197, v196, v137
	v_pk_mul_f32 v[136:137], v[202:203], s[56:57]
	v_fmac_f32_e32 v195, v194, v132
	v_fmac_f32_e32 v137, v136, v133
	v_lshl_add_u64 v[132:133], s[62:63], 0, v[186:187]
	v_lshl_add_u64 v[178:179], v[132:133], 0, v[178:179]
	v_cvt_pk_bf16_f32 v130, v191, v193
	v_cvt_pk_bf16_f32 v131, v131, v197
	v_cvt_pk_bf16_f32 v132, v199, v135
	v_cvt_pk_bf16_f32 v133, v195, v137
	global_store_dwordx4 v[178:179], v[130:133], off
	global_load_dwordx4 v[130:133], v[140:141], off offset:16
	s_nop 0
	global_load_dwordx4 v[134:137], v[140:141], off
	v_lshl_add_u64 v[140:141], s[6:7], 0, v[182:183]
	v_lshl_add_u64 v[140:141], v[140:141], 0, v[138:139]
	v_lshl_add_u64 v[144:145], s[6:7], 0, v[144:145]
	global_load_dwordx4 v[190:193], v[140:141], off
	v_lshl_add_u64 v[144:145], v[144:145], 0, v[138:139]
	global_load_dwordx4 v[194:197], v[144:145], off
	v_lshl_add_u64 v[140:141], s[6:7], 0, v[142:143]
	v_lshl_add_u64 v[140:141], v[140:141], 0, v[138:139]
	global_load_dwordx4 v[140:143], v[140:141], off
	v_lshl_add_u64 v[144:145], s[6:7], 0, v[186:187]
	v_lshl_add_u64 v[138:139], v[144:145], 0, v[138:139]
	global_load_dwordx4 v[198:201], v[138:139], off
	v_mov_b32_e32 v138, v66
	v_mov_b32_e32 v144, v67
	v_mov_b32_e32 v202, v55
	v_mov_b32_e32 v182, v68
	v_mov_b32_e32 v204, v56
	v_mov_b32_e32 v186, v69
	s_waitcnt vmcnt(0)
	v_lshlrev_b32_e32 v139, 16, v190
	v_and_b32_e32 v145, 0xffff0000, v190
	v_lshlrev_b32_e32 v183, 16, v191
	v_and_b32_e32 v187, 0xffff0000, v191
	v_lshlrev_b32_e32 v191, 16, v192
	v_and_b32_e32 v203, 0xffff0000, v192
	v_lshlrev_b32_e32 v205, 16, v193
	v_and_b32_e32 v193, 0xffff0000, v193
	v_mov_b32_e32 v192, v57
	v_pk_mul_f32 v[138:139], v[138:139], s[56:57]
	v_mov_b32_e32 v190, v54
	v_pk_mul_f32 v[144:145], v[144:145], s[56:57]
	v_pk_mul_f32 v[192:193], v[192:193], s[56:57]
	v_fmac_f32_e32 v139, v138, v134
	v_pk_mul_f32 v[206:207], v[190:191], s[56:57]
	v_fmac_f32_e32 v145, v144, v135
	v_pk_mul_f32 v[202:203], v[202:203], s[56:57]
	v_pk_mul_f32 v[182:183], v[182:183], s[56:57]
	v_pk_mul_f32 v[204:205], v[204:205], s[56:57]
	v_pk_mul_f32 v[186:187], v[186:187], s[56:57]
	v_fmac_f32_e32 v193, v192, v133
	v_fmac_f32_e32 v207, v206, v130
	v_fmac_f32_e32 v203, v202, v131
	v_fmac_f32_e32 v183, v182, v136
	v_fmac_f32_e32 v205, v204, v132
	v_fmac_f32_e32 v187, v186, v137
	v_cvt_pk_bf16_f32 v190, v139, v145
	v_cvt_pk_bf16_f32 v191, v183, v187
	v_cvt_pk_bf16_f32 v192, v207, v203
	v_cvt_pk_bf16_f32 v193, v205, v193
	global_store_dwordx4 v[180:181], v[190:193], off offset:256
	v_lshlrev_b32_e32 v139, 16, v140
	v_and_b32_e32 v145, 0xffff0000, v140
	v_lshlrev_b32_e32 v181, 16, v141
	v_and_b32_e32 v141, 0xffff0000, v141
	v_mov_b32_e32 v138, v42
	v_mov_b32_e32 v140, v45
	v_lshlrev_b32_e32 v183, 16, v142
	v_and_b32_e32 v187, 0xffff0000, v142
	v_lshlrev_b32_e32 v191, 16, v143
	v_and_b32_e32 v143, 0xffff0000, v143
	v_pk_mul_f32 v[138:139], v[138:139], s[56:57]
	v_mov_b32_e32 v182, v34
	v_mov_b32_e32 v144, v43
	v_mov_b32_e32 v186, v35
	v_mov_b32_e32 v180, v44
	v_mov_b32_e32 v190, v36
	v_pk_mul_f32 v[140:141], v[140:141], s[56:57]
	v_mov_b32_e32 v142, v37
	v_fmac_f32_e32 v139, v138, v134
	v_pk_mul_f32 v[182:183], v[182:183], s[56:57]
	v_pk_mul_f32 v[144:145], v[144:145], s[56:57]
	v_pk_mul_f32 v[186:187], v[186:187], s[56:57]
	v_pk_mul_f32 v[180:181], v[180:181], s[56:57]
	v_pk_mul_f32 v[190:191], v[190:191], s[56:57]
	v_fmac_f32_e32 v141, v140, v137
	v_pk_mul_f32 v[142:143], v[142:143], s[56:57]
	v_fmac_f32_e32 v183, v182, v130
	v_fmac_f32_e32 v145, v144, v135
	v_fmac_f32_e32 v187, v186, v131
	v_fmac_f32_e32 v181, v180, v136
	v_fmac_f32_e32 v191, v190, v132
	v_fmac_f32_e32 v143, v142, v133
	v_cvt_pk_bf16_f32 v138, v139, v145
	v_cvt_pk_bf16_f32 v139, v181, v141
	v_cvt_pk_bf16_f32 v140, v183, v187
	v_cvt_pk_bf16_f32 v141, v191, v143
	global_store_dwordx4 v[184:185], v[138:141], off offset:256
	v_lshlrev_b32_e32 v143, 16, v195
	v_and_b32_e32 v145, 0xffff0000, v195
	v_lshlrev_b32_e32 v139, 16, v194
	v_and_b32_e32 v141, 0xffff0000, v194
	v_mov_b32_e32 v138, v26
	v_mov_b32_e32 v140, v27
	v_lshlrev_b32_e32 v181, 16, v196
	v_and_b32_e32 v183, 0xffff0000, v196
	v_lshlrev_b32_e32 v185, 16, v197
	v_and_b32_e32 v187, 0xffff0000, v197
	v_pk_mul_f32 v[138:139], v[138:139], s[56:57]
	v_mov_b32_e32 v180, v18
	v_pk_mul_f32 v[140:141], v[140:141], s[56:57]
	v_mov_b32_e32 v182, v19
	v_mov_b32_e32 v142, v28
	v_mov_b32_e32 v184, v20
	v_mov_b32_e32 v144, v29
	v_mov_b32_e32 v186, v21
	v_fmac_f32_e32 v139, v138, v134
	v_pk_mul_f32 v[180:181], v[180:181], s[56:57]
	v_fmac_f32_e32 v141, v140, v135
	v_pk_mul_f32 v[182:183], v[182:183], s[56:57]
	v_pk_mul_f32 v[142:143], v[142:143], s[56:57]
	v_pk_mul_f32 v[184:185], v[184:185], s[56:57]
	v_pk_mul_f32 v[144:145], v[144:145], s[56:57]
	v_pk_mul_f32 v[186:187], v[186:187], s[56:57]
	v_fmac_f32_e32 v181, v180, v130
	v_fmac_f32_e32 v183, v182, v131
	v_fmac_f32_e32 v143, v142, v136
	v_fmac_f32_e32 v185, v184, v132
	v_fmac_f32_e32 v145, v144, v137
	v_fmac_f32_e32 v187, v186, v133
	v_cvt_pk_bf16_f32 v138, v139, v141
	v_cvt_pk_bf16_f32 v139, v143, v145
	v_cvt_pk_bf16_f32 v140, v181, v183
	v_cvt_pk_bf16_f32 v141, v185, v187
	global_store_dwordx4 v[188:189], v[138:141], off offset:256
	v_lshlrev_b32_e32 v181, 16, v200
	v_and_b32_e32 v183, 0xffff0000, v200
	v_lshlrev_b32_e32 v139, 16, v198
	v_and_b32_e32 v141, 0xffff0000, v198
	v_mov_b32_e32 v138, v10
	v_mov_b32_e32 v140, v11
	v_pk_mul_f32 v[138:139], v[138:139], s[56:57]
	v_mov_b32_e32 v180, v2
	v_pk_mul_f32 v[140:141], v[140:141], s[56:57]
	v_mov_b32_e32 v182, v3
	v_lshlrev_b32_e32 v143, 16, v199
	v_and_b32_e32 v145, 0xffff0000, v199
	v_fmac_f32_e32 v139, v138, v134
	v_pk_mul_f32 v[180:181], v[180:181], s[56:57]
	v_fmac_f32_e32 v141, v140, v135
	v_pk_mul_f32 v[134:135], v[182:183], s[56:57]
	v_mov_b32_e32 v142, v12
	v_mov_b32_e32 v144, v13
	v_lshlrev_b32_e32 v185, 16, v201
	v_and_b32_e32 v187, 0xffff0000, v201
	v_fmac_f32_e32 v181, v180, v130
	v_fmac_f32_e32 v135, v134, v131
	v_pk_mul_f32 v[130:131], v[142:143], s[56:57]
	v_mov_b32_e32 v184, v4
	v_pk_mul_f32 v[144:145], v[144:145], s[56:57]
	v_mov_b32_e32 v186, v5
	v_fmac_f32_e32 v131, v130, v136
	v_pk_mul_f32 v[142:143], v[184:185], s[56:57]
	v_fmac_f32_e32 v145, v144, v137
	v_pk_mul_f32 v[136:137], v[186:187], s[56:57]
	v_fmac_f32_e32 v143, v142, v132
	v_fmac_f32_e32 v137, v136, v133
	v_cvt_pk_bf16_f32 v130, v139, v141
	v_cvt_pk_bf16_f32 v131, v131, v145
	v_cvt_pk_bf16_f32 v132, v181, v135
	v_cvt_pk_bf16_f32 v133, v143, v137
	global_store_dwordx4 v[178:179], v[130:133], off offset:256
.LBB0_3627:
	s_andn2_b64 vcc, exec, vcc
	s_cbranch_vccnz .LBB0_3619
	s_waitcnt lgkmcnt(0)
	v_cmp_lt_i32_e32 vcc, -1, v177
	s_and_saveexec_b64 s[12:13], vcc
	s_cbranch_execnz .LBB0_3639
	s_or_b64 exec, exec, s[12:13]
	v_cmp_lt_i32_e32 vcc, -1, v175
	s_and_saveexec_b64 s[12:13], vcc
	s_cbranch_execnz .LBB0_3640
